# row-constant staging in front of LN1: four loads in flight with counted waits instead of four load-wait-write round trips
# baseline (speedup 1.0000x reference)
; #define LAS __attribute__((address_space(3)))
; __global__ void __launch_bounds__(NW * 64, 2) mk_fwd(Args args) {
;     ...
;             if (tid2 < 256) { const int i = tid2 * 4; *(LAS f32x4*)(cv + i) = *(const f32x4*)(X.ln1_g + i); *(LAS f32x4*)(cv + 1024 + i) = *(const f32x4*)(X.ln1_b + i);
;                 *(LAS f32x4*)(cv + 2048 + i) = *(const f32x4*)(mod + b * 6144 + MOD_SCALE_F + i) + 1.f; *(LAS f32x4*)(cv + 3072 + i) = *(const f32x4*)(mod + b * 6144 + MOD_SHIFT_F + i); }
;             __syncthreads();
.LBB0_412:
	s_waitcnt vmcnt(0)
	s_barrier
	s_waitcnt vmcnt(0)
	v_mov_b32_e32 v0, v196
	s_barrier
	s_movk_i32 s69, 0x100
	v_add_u32_e32 v1, s91, v0
	v_cmp_gt_i32_e32 vcc, s69, v1
	s_and_saveexec_b64 s[4:5], vcc
	s_cbranch_execz .LBB0_414
	v_readlane_b32 s12, v252, 8
	v_readlane_b32 s13, v252, 9
	s_load_dwordx4 s[8:11], s[12:13], 0x48
	v_lshlrev_b32_e32 v2, 2, v1
	v_ashrrev_i32_e32 v3, 31, v2
	v_lshlrev_b64 v[6:7], 2, v[2:3]
	v_lshl_add_u32 v1, v1, 4, 0
	s_lshr_b32 s6, s2, 3
	s_mulk_i32 s6, 0x1800
	s_ashr_i32 s7, s6, 31
	s_lshl_b64 s[6:7], s[6:7], 2
	s_add_u32 s6, s85, s6
	s_addc_u32 s7, s87, s7
	s_waitcnt lgkmcnt(0)
	v_lshl_add_u64 v[2:3], s[8:9], 0, v[6:7]
	global_load_dwordx4 v[32:35], v[2:3], off
	v_lshl_add_u64 v[8:9], s[10:11], 0, v[6:7]
	global_load_dwordx4 v[36:39], v[8:9], off
	v_lshl_add_u64 v[6:7], s[6:7], 0, v[6:7]
	v_add_co_u32_e32 v10, vcc, s40, v6
	s_nop 1
	v_addc_co_u32_e32 v11, vcc, 0, v7, vcc
	global_load_dwordx4 v[40:43], v[10:11], off
	v_add_co_u32_e32 v12, vcc, 0x3000, v6
	s_nop 1
	v_addc_co_u32_e32 v13, vcc, 0, v7, vcc
	global_load_dwordx4 v[44:47], v[12:13], off
	s_waitcnt vmcnt(3)
	ds_write_b128 v1, v[32:35]
	s_waitcnt vmcnt(2)
	ds_write_b128 v1, v[36:39] offset:4096
	s_waitcnt vmcnt(1)
	v_pk_add_f32 v[42:43], v[42:43], 1.0 op_sel_hi:[1,0]
	v_pk_add_f32 v[40:41], v[40:41], 1.0 op_sel_hi:[1,0]
	ds_write_b128 v1, v[40:43] offset:8192
	s_waitcnt vmcnt(0)
	ds_write_b128 v1, v[44:47] offset:12288
